# speedup vs baseline: 1.0090x; 1.0090x over previous
_Z11main_kernelPKfPKiPK15HIP_vector_typeIjLj4EES0_PfS7_S2_i:
	v_and_b32_e32 v104, 0x3ff, v0
	s_mul_i32 s2, s2, 12
	v_readfirstlane_b32 s3, v104
	s_lshr_b32 s3, s3, 6
	s_add_i32 s2, s3, s2
	s_load_dwordx8 s[12:19], s[0:1], 0x0
	s_load_dwordx2 s[10:11], s[0:1], 0x30
	s_mul_i32 s2, s2, 0xf424
	s_mul_hi_u32 s4, s2, 0xaaaaaaab
	s_add_i32 s2, s2, 0xf424
	s_mul_hi_u32 s2, s2, 0xaaaaaaab
	s_lshr_b32 s42, s2, 11
	s_lshl_b32 s2, s3, 8
	v_and_b32_e32 v1, 15, v0
	v_bfe_u32 v112, v0, 4, 2
	s_lshr_b32 s44, s4, 11
	s_lshl_b32 s33, s3, 13
	s_add_i32 s43, s2, 0x20000
	s_cmp_lt_u32 s33, 0xc000
	s_cbranch_scc1 .Lmain_older
	s_setprio 1
.Lmain_older:
	s_sub_u32 s60, s42, s44
	s_cmp_lt_u32 s60, 21
	s_cbranch_scc1 .Lmain_noprio
	s_setprio 2
